# hosted value-table conversion software-pipelined: quantise the row requested one tile earlier, then request the next (on top of v4)
# speedup vs baseline: 1.0136x; 1.0041x over previous
.LBB0_1806:
	s_or_b64 exec, exec, s[12:13]
	s_cmpk_gt_u32 s2, 0x7ff
	s_cbranch_scc1 .LBB0_1936
	s_add_u32 s42, s8, 0x40400000
	s_addc_u32 s43, s9, 0
	s_add_u32 s50, s10, 4.0
	s_addc_u32 s51, s11, 0
	s_ashr_i32 s8, s18, 6
	s_lshr_b32 s47, s2, 3
	s_lshl_b32 s9, s3, 9
	v_and_b32_e32 v35, 15, v5
	s_add_u32 s6, s6, s9
	s_addc_u32 s7, s7, 0
	v_lshlrev_b32_e32 v36, 5, v35
	v_mov_b32_e32 v37, 0
	v_lshl_add_u64 v[2:3], s[6:7], 0, v[36:37]
	s_mov_b64 s[6:7], 0x38400000
	v_ashrrev_i32_e32 v72, 4, v5
	v_lshl_add_u64 v[38:39], v[2:3], 0, s[6:7]
	s_movk_i32 s6, 0x210
	v_mul_lo_u32 v2, v72, s6
	s_add_i32 s6, 0, 0x11000
	v_and_b32_e32 v4, 48, v5
	v_add_u32_e32 v2, s6, v2
	v_add_u32_e32 v6, 0, v4
	v_add_u32_e32 v4, s6, v4
	s_lshl_b32 s6, s8, 10
	s_add_i32 s6, s6, 0
	v_lshrrev_b32_e32 v7, 2, v5
	s_add_i32 s6, s6, 0x1d600
	v_bfe_u32 v5, v5, 4, 2
	v_lshl_add_u32 v73, v5, 8, s6
	v_lshl_or_b32 v74, s8, 2, v5
	s_movk_i32 s6, 0x420
	v_lshl_or_b32 v3, s8, 4, v35
	v_and_b32_e32 v7, 12, v7
	v_mul_lo_u32 v5, v74, s6
	s_add_i32 s6, 0, 0x15200
	v_lshlrev_b32_e32 v8, 2, v35
	s_movk_i32 s7, 0x110
	v_add3_u32 v75, s6, v5, v8
	v_lshlrev_b32_e32 v5, 3, v35
	v_mul_lo_u32 v8, v3, s7
	v_lshl_add_u32 v3, v3, 2, s6
	v_mul_u32_u24_e32 v9, 0x210, v35
	v_mul_u32_u24_e32 v7, 0x420, v7
	s_lshl_b32 s52, s3, 4
	v_or_b32_e32 v41, 16, v35
	v_or_b32_e32 v43, 32, v35
	v_or_b32_e32 v45, 48, v35
	v_or_b32_e32 v47, 64, v35
	v_or_b32_e32 v49, 0x50, v35
	v_or_b32_e32 v51, 0x60, v35
	v_or_b32_e32 v53, 0x70, v35
	s_lshr_b32 s53, s46, 3
	v_add_u32_e32 v76, v2, v36
	v_add_u32_e32 v77, v6, v8
	v_add_u32_e32 v78, v4, v9
	v_add_u32_e32 v79, v3, v7
	v_add_u32_e32 v80, v73, v5
	s_mov_b32 s54, 0x800000
	s_mov_b32 s55, 0xff000000
	s_load_dwordx2 s[94:95], s[0:1], 0x80
	s_load_dwordx2 s[96:97], s[0:1], 0x90
	v_lshlrev_b32_e32 v226, 4, v1
	v_mov_b32_e32 v227, 0
	v_lshlrev_b32_e32 v228, 2, v1
	v_ashrrev_i32_e32 v232, 6, v0
	v_mov_b32_e32 v233, 0x260
	v_mov_b32_e32 v234, 0x41700000
	s_waitcnt lgkmcnt(0)
	s_add_u32 s98, s96, 0x16300000
	s_addc_u32 s99, s97, 0
	s_add_u32 s96, s96, 0x12300000
	s_addc_u32 s97, s97, 0
	s_mov_b32 s60, s47
	s_lshr_b32 s60, s60, 5
	s_lshl_b32 s61, s2, 3
	s_add_i32 s60, s60, s61
	s_addk_i32 s60, 0x800
	v_mov_b32_e32 v162, s60
	s_mov_b64 s[62:63], s[94:95]
	s_mov_b64 s[64:65], s[94:95]
	s_movk_i32 s72, 0x1000
	s_movk_i32 s73, 0x3fff
	s_movk_i32 s74, 0x2000
	s_movk_i32 s75, 0x3000
	v_lshl_add_u32 v162, v162, 3, v232
	v_add_u32_e32 v163, 0xffffc000, v162
	v_cmp_lt_i32_e64 s[86:87], s73, v162
	v_mov_b32_e32 v164, s64
	s_nop 0
	v_cndmask_b32_e64 v230, v162, v163, s[86:87]
	v_mov_b32_e32 v162, s63
	v_mov_b32_e32 v163, s65
	v_cndmask_b32_e64 v163, v162, v163, s[86:87]
	v_mov_b32_e32 v162, s62
	v_ashrrev_i32_e32 v231, 31, v230
	v_cndmask_b32_e64 v162, v162, v164, s[86:87]
	v_lshlrev_b64 v[164:165], 14, v[230:231]
	v_lshl_add_u64 v[162:163], v[162:163], 0, v[164:165]
	v_lshl_add_u64 v[162:163], v[162:163], 0, v[226:227]
	v_add_co_u32_e32 v194, vcc, s74, v162
	global_load_dwordx4 v[206:209], v[162:163], off
	global_load_dwordx4 v[190:193], v[162:163], off offset:1024
	global_load_dwordx4 v[186:189], v[162:163], off offset:2048
	global_load_dwordx4 v[178:181], v[162:163], off offset:3072
	v_addc_co_u32_e32 v195, vcc, 0, v163, vcc
	global_load_dwordx4 v[182:185], v[194:195], off offset:-4096
	v_add_co_u32_e32 v164, vcc, s72, v162
	s_nop 0
	s_nop 0
	v_addc_co_u32_e32 v165, vcc, 0, v163, vcc
	global_load_dwordx4 v[170:173], v[164:165], off offset:1024
	v_add_co_u32_e32 v196, vcc, s75, v162
	s_nop 0
	s_nop 0
	v_addc_co_u32_e32 v197, vcc, 0, v163, vcc
	global_load_dwordx4 v[222:225], v[164:165], off offset:2048
	global_load_dwordx4 v[210:213], v[164:165], off offset:3072
	global_load_dwordx4 v[198:201], v[194:195], off
	global_load_dwordx4 v[174:177], v[194:195], off offset:1024
	global_load_dwordx4 v[166:169], v[194:195], off offset:2048
	s_nop 0
	global_load_dwordx4 v[162:165], v[196:197], off offset:3072
	global_load_dwordx4 v[86:89], v[194:195], off offset:3072
	global_load_dwordx4 v[90:93], v[196:197], off
	global_load_dwordx4 v[94:97], v[196:197], off offset:1024
	global_load_dwordx4 v[98:101], v[196:197], off offset:2048
	s_branch .LBB0_1809

.LBB0_1809:
	s_lshl_b32 s56, s47, 5
	v_add_u32_e32 v2, s56, v72
	v_ashrrev_i32_e32 v3, 31, v2
	v_lshlrev_b64 v[2:3], 12, v[2:3]
	v_lshl_add_u64 v[10:11], v[38:39], 0, v[2:3]
	s_waitcnt lgkmcnt(0)
	s_barrier
	global_load_dwordx4 v[2:5], v[10:11], off
	global_load_dwordx4 v[6:9], v[10:11], off offset:16
	s_waitcnt vmcnt(1)
	ds_write_b128 v76, v[2:5]
	s_waitcnt vmcnt(0)
	ds_write_b128 v76, v[6:9] offset:16
	s_waitcnt vmcnt(0) lgkmcnt(0)
	s_mov_b32 s60, s96
	s_mov_b32 s61, s97
	s_mov_b64 s[66:67], s[98:99]
	s_mov_b64 s[68:69], s[96:97]
	s_mov_b64 s[70:71], s[98:99]
	s_movk_i32 s72, 0x1000
	s_movk_i32 s73, 0x3fff
	s_movk_i32 s74, 0x2000
	s_movk_i32 s75, 0x3000
	s_mov_b32 s76, 0xf800000
	s_mov_b32 s77, 0x8080808
	s_mov_b32 s78, 0x400000
	s_mov_b32 s79, 0x800000
	s_mov_b32 s80, 0xc00000
	s_mov_b32 s81, 0x1000000
	v_cmp_eq_u32_e64 s[82:83], 0, v1
	s_mov_b64 s[86:87], exec
	v_mul_f32_e32 v202, v207, v207
	v_mul_f32_e32 v203, v209, v209
	v_max_f32_e64 v204, |v207|, |v207|
	v_max_f32_e64 v205, |v206|, |v206|
	v_max_f32_e64 v214, |v209|, |v209|
	v_max_f32_e64 v215, |v208|, |v208|
	s_nop 0
	v_mul_f32_e32 v216, v191, v191
	v_mul_f32_e32 v217, v193, v193
	s_nop 0
	v_mul_f32_e32 v229, v187, v187
	v_mul_f32_e32 v235, v189, v189
	v_fmac_f32_e32 v202, v206, v206
	v_fmac_f32_e32 v203, v208, v208
	v_max_f32_e32 v204, v205, v204
	v_max_f32_e32 v205, v215, v214
	v_fmac_f32_e32 v216, v190, v190
	v_fmac_f32_e32 v217, v192, v192
	v_max_f32_e64 v218, |v191|, |v191|
	v_max_f32_e64 v219, |v190|, |v190|
	v_max_f32_e64 v236, |v187|, |v187|
	v_max_f32_e64 v237, |v186|, |v186|
	s_nop 0
	v_mul_f32_e32 v240, v179, v179
	v_mul_f32_e32 v241, v181, v181
	v_fmac_f32_e32 v229, v186, v186
	v_fmac_f32_e32 v235, v188, v188
	v_add_f32_e32 v202, v202, v203
	v_max3_f32 v203, v204, 0, v205
	v_add_f32_e32 v204, v216, v217
	v_max_f32_e32 v214, v219, v218
	v_max_f32_e32 v218, v237, v236
	v_fmac_f32_e32 v240, v178, v178
	v_fmac_f32_e32 v241, v180, v180
	s_nop 0
	v_mul_f32_e32 v236, v183, v183
	v_mul_f32_e32 v237, v185, v185
	v_add_f32_e32 v205, v229, v235
	v_add_f32_e32 v202, v202, v204
	v_max_f32_e64 v220, |v193|, |v193|
	v_max_f32_e64 v221, |v192|, |v192|
	v_add_f32_e32 v216, v240, v241
	v_fmac_f32_e32 v236, v182, v182
	v_fmac_f32_e32 v237, v184, v184
	v_add_f32_e32 v202, v202, v205
	v_max_f32_e64 v238, |v189|, |v189|
	v_max_f32_e64 v239, |v188|, |v188|
	v_max_f32_e32 v215, v221, v220
	v_add_f32_e32 v202, v202, v216
	v_add_f32_e32 v204, v236, v237
	v_max_f32_e64 v242, |v179|, |v179|
	v_max_f32_e64 v243, |v178|, |v178|
	v_max_f32_e64 v244, |v181|, |v181|
	v_max_f32_e64 v245, |v180|, |v180|
	v_max_f32_e32 v219, v239, v238
	v_max3_f32 v203, v203, v214, v215
	v_add_f32_e32 v202, v202, v204
	v_max_f32_e64 v204, |v183|, |v183|
	v_max_f32_e64 v205, |v182|, |v182|
	v_max_f32_e32 v220, v243, v242
	v_max_f32_e32 v221, v245, v244
	v_max3_f32 v203, v203, v218, v219
	v_max_f32_e32 v204, v205, v204
	v_max_f32_e64 v205, |v185|, |v185|
	v_max_f32_e64 v214, |v184|, |v184|
	v_max3_f32 v203, v203, v220, v221
	v_max_f32_e32 v205, v214, v205
	v_max3_f32 v203, v203, v204, v205
	v_mov_b32_e32 v218, v86
	v_mov_b32_e32 v219, v87
	v_mov_b32_e32 v220, v88
	v_mov_b32_e32 v221, v89
	v_mov_b32_e32 v214, v90
	v_mov_b32_e32 v215, v91
	v_mov_b32_e32 v216, v92
	v_mov_b32_e32 v217, v93
	v_cmp_lt_i32_e32 vcc, v157, v154
	s_nop 0
	v_mul_f32_e32 v204, v171, v171
	v_mul_f32_e32 v194, v173, v173
	v_fmac_f32_e32 v204, v170, v170
	v_fmac_f32_e32 v194, v172, v172
	v_add_f32_e32 v194, v204, v194
	v_add_f32_e32 v194, v202, v194
	v_max_f32_e64 v195, |v171|, |v171|
	v_max_f32_e64 v202, |v170|, |v170|
	v_max_f32_e32 v195, v202, v195
	v_max_f32_e64 v202, |v173|, |v173|
	v_max_f32_e64 v204, |v172|, |v172|
	v_max_f32_e32 v202, v204, v202
	v_max3_f32 v195, v203, v195, v202
	s_nop 0
	v_mul_f32_e32 v202, v223, v223
	v_mul_f32_e32 v203, v225, v225
	v_fmac_f32_e32 v202, v222, v222
	v_fmac_f32_e32 v203, v224, v224
	v_add_f32_e32 v202, v202, v203
	v_add_f32_e32 v194, v194, v202
	v_max_f32_e64 v202, |v223|, |v223|
	v_max_f32_e64 v203, |v222|, |v222|
	v_max_f32_e32 v202, v203, v202
	v_max_f32_e64 v203, |v225|, |v225|
	v_max_f32_e64 v204, |v224|, |v224|
	v_max_f32_e32 v203, v204, v203
	v_max3_f32 v229, v195, v202, v203
	v_mov_b32_e32 v202, v94
	v_mov_b32_e32 v203, v95
	v_mov_b32_e32 v204, v96
	v_mov_b32_e32 v205, v97
	s_nop 0
	v_mul_f32_e32 v195, v211, v211
	v_mul_f32_e32 v235, v213, v213
	v_fmac_f32_e32 v195, v210, v210
	v_fmac_f32_e32 v235, v212, v212
	v_add_f32_e32 v195, v195, v235
	v_add_f32_e32 v235, v194, v195
	v_max_f32_e64 v194, |v211|, |v211|
	v_max_f32_e64 v195, |v210|, |v210|
	v_max_f32_e32 v236, v195, v194
	v_max_f32_e64 v194, |v213|, |v213|
	v_max_f32_e64 v195, |v212|, |v212|
	v_max_f32_e32 v237, v195, v194
	v_mov_b32_e32 v194, v98
	v_mov_b32_e32 v195, v99
	v_mov_b32_e32 v196, v100
	v_mov_b32_e32 v197, v101
	v_max3_f32 v229, v229, v236, v237
	s_nop 0
	v_mul_f32_e32 v236, v199, v199
	v_mul_f32_e32 v237, v201, v201
	v_fmac_f32_e32 v236, v198, v198
	v_fmac_f32_e32 v237, v200, v200
	v_add_f32_e32 v236, v236, v237
	v_add_f32_e32 v235, v235, v236
	v_max_f32_e64 v236, |v199|, |v199|
	v_max_f32_e64 v237, |v198|, |v198|
	v_max_f32_e32 v236, v237, v236
	v_max_f32_e64 v237, |v201|, |v201|
	v_max_f32_e64 v238, |v200|, |v200|
	v_max_f32_e32 v237, v238, v237
	v_max3_f32 v229, v229, v236, v237
	s_nop 0
	v_mul_f32_e32 v236, v175, v175
	v_mul_f32_e32 v237, v177, v177
	v_fmac_f32_e32 v236, v174, v174
	v_fmac_f32_e32 v237, v176, v176
	v_add_f32_e32 v236, v236, v237
	v_add_f32_e32 v235, v235, v236
	v_max_f32_e64 v236, |v175|, |v175|
	v_max_f32_e64 v237, |v174|, |v174|
	v_max_f32_e32 v236, v237, v236
	v_max_f32_e64 v237, |v177|, |v177|
	v_max_f32_e64 v238, |v176|, |v176|
	v_max_f32_e32 v237, v238, v237
	v_max3_f32 v229, v229, v236, v237
	s_nop 0
	v_mul_f32_e32 v236, v167, v167
	v_mul_f32_e32 v237, v169, v169
	v_fmac_f32_e32 v236, v166, v166
	v_fmac_f32_e32 v237, v168, v168
	v_add_f32_e32 v236, v236, v237
	v_add_f32_e32 v235, v235, v236
	v_max_f32_e64 v236, |v167|, |v167|
	v_max_f32_e64 v237, |v166|, |v166|
	v_max_f32_e32 v236, v237, v236
	v_max_f32_e64 v237, |v169|, |v169|
	v_max_f32_e64 v238, |v168|, |v168|
	v_max_f32_e32 v237, v238, v237
	v_max3_f32 v229, v229, v236, v237
	s_nop 0
	v_mul_f32_e32 v236, v219, v219
	v_mul_f32_e32 v237, v221, v221
	v_fmac_f32_e32 v236, v218, v218
	v_fmac_f32_e32 v237, v220, v220
	v_add_f32_e32 v236, v236, v237
	v_add_f32_e32 v235, v235, v236
	v_max_f32_e64 v236, |v219|, |v219|
	v_max_f32_e64 v237, |v218|, |v218|
	v_max_f32_e32 v236, v237, v236
	v_max_f32_e64 v237, |v221|, |v221|
	v_max_f32_e64 v238, |v220|, |v220|
	v_max_f32_e32 v237, v238, v237
	v_max3_f32 v229, v229, v236, v237
	s_nop 0
	v_mul_f32_e32 v236, v215, v215
	v_mul_f32_e32 v237, v217, v217
	v_fmac_f32_e32 v236, v214, v214
	v_fmac_f32_e32 v237, v216, v216
	v_add_f32_e32 v236, v236, v237
	v_add_f32_e32 v235, v235, v236
	v_max_f32_e64 v236, |v215|, |v215|
	v_max_f32_e64 v237, |v214|, |v214|
	v_max_f32_e32 v236, v237, v236
	v_max_f32_e64 v237, |v217|, |v217|
	v_max_f32_e64 v238, |v216|, |v216|
	v_max_f32_e32 v237, v238, v237
	v_max3_f32 v229, v229, v236, v237
	s_nop 0
	v_mul_f32_e32 v236, v203, v203
	v_mul_f32_e32 v237, v205, v205
	v_fmac_f32_e32 v236, v202, v202
	v_fmac_f32_e32 v237, v204, v204
	v_add_f32_e32 v236, v236, v237
	v_add_f32_e32 v235, v235, v236
	v_max_f32_e64 v236, |v203|, |v203|
	v_max_f32_e64 v237, |v202|, |v202|
	v_max_f32_e32 v236, v237, v236
	v_max_f32_e64 v237, |v205|, |v205|
	v_max_f32_e64 v238, |v204|, |v204|
	v_max_f32_e32 v237, v238, v237
	v_max3_f32 v229, v229, v236, v237
	s_nop 0
	v_mul_f32_e32 v236, v195, v195
	v_mul_f32_e32 v237, v197, v197
	v_fmac_f32_e32 v236, v194, v194
	v_fmac_f32_e32 v237, v196, v196
	v_add_f32_e32 v236, v236, v237
	v_add_f32_e32 v235, v235, v236
	v_max_f32_e64 v236, |v195|, |v195|
	v_max_f32_e64 v237, |v194|, |v194|
	v_max_f32_e32 v236, v237, v236
	v_max_f32_e64 v237, |v197|, |v197|
	v_max_f32_e64 v238, |v196|, |v196|
	v_max_f32_e32 v237, v238, v237
	v_max3_f32 v229, v229, v236, v237
	v_mul_f32_e32 v236, v163, v163
	v_mul_f32_e32 v237, v165, v165
	v_fmac_f32_e32 v236, v162, v162
	v_fmac_f32_e32 v237, v164, v164
	v_add_f32_e32 v236, v236, v237
	v_add_f32_e32 v235, v235, v236
	v_max_f32_e64 v236, |v163|, |v163|
	v_max_f32_e64 v237, |v162|, |v162|
	v_max_f32_e32 v236, v237, v236
	v_max_f32_e64 v237, |v165|, |v165|
	v_max_f32_e64 v240, |v164|, |v164|
	v_cndmask_b32_e32 v238, v1, v157, vcc
	v_max_f32_e32 v237, v240, v237
	v_lshlrev_b32_e32 v238, 2, v238
	v_max3_f32 v229, v229, v236, v237
	ds_bpermute_b32 v239, v238, v235
	ds_bpermute_b32 v236, v238, v229
	v_cmp_lt_i32_e32 vcc, v158, v154
	s_waitcnt lgkmcnt(1)
	v_add_f32_e32 v235, v235, v239
	v_cndmask_b32_e32 v237, v1, v158, vcc
	v_lshlrev_b32_e32 v237, 2, v237
	s_waitcnt lgkmcnt(0)
	v_max_f32_e32 v236, v236, v236
	ds_bpermute_b32 v238, v237, v235
	v_max_f32_e32 v229, v229, v236
	ds_bpermute_b32 v236, v237, v229
	v_cmp_lt_i32_e32 vcc, v159, v154
	s_waitcnt lgkmcnt(1)
	v_add_f32_e32 v235, v235, v238
	v_cndmask_b32_e32 v237, v1, v159, vcc
	v_lshlrev_b32_e32 v237, 2, v237
	ds_bpermute_b32 v238, v237, v235
	s_waitcnt lgkmcnt(1)
	v_max_f32_e32 v236, v236, v236
	v_max_f32_e32 v229, v229, v236
	ds_bpermute_b32 v236, v237, v229
	v_cmp_lt_i32_e32 vcc, v160, v154
	s_waitcnt lgkmcnt(1)
	v_add_f32_e32 v235, v235, v238
	s_waitcnt lgkmcnt(0)
	v_max_f32_e32 v236, v236, v236
	v_cndmask_b32_e32 v237, v1, v160, vcc
	v_lshlrev_b32_e32 v237, 2, v237
	ds_bpermute_b32 v238, v237, v235
	v_max_f32_e32 v229, v229, v236
	ds_bpermute_b32 v236, v237, v229
	v_cmp_lt_i32_e32 vcc, v156, v154
	s_waitcnt lgkmcnt(1)
	v_add_f32_e32 v235, v235, v238
	v_cndmask_b32_e32 v237, v1, v156, vcc
	v_lshlrev_b32_e32 v237, 2, v237
	ds_bpermute_b32 v238, v237, v235
	s_waitcnt lgkmcnt(1)
	v_max_f32_e32 v236, v236, v236
	v_max_f32_e32 v229, v229, v236
	v_cmp_lt_i32_e32 vcc, v155, v154
	ds_bpermute_b32 v236, v237, v229
	s_waitcnt lgkmcnt(1)
	v_add_f32_e32 v235, v235, v238
	v_cndmask_b32_e32 v237, v1, v155, vcc
	v_lshlrev_b32_e32 v237, 2, v237
	ds_bpermute_b32 v238, v237, v235
	s_waitcnt lgkmcnt(1)
	v_max_f32_e32 v236, v236, v236
	v_max_f32_e32 v229, v229, v236
	ds_bpermute_b32 v236, v237, v229
	s_waitcnt lgkmcnt(1)
	v_add_f32_e32 v235, v235, v238
	v_mul_f32_e32 v235, 0x39800000, v235
	v_mul_f32_e32 v237, 0x4f800000, v235
	v_cmp_gt_f32_e32 vcc, s76, v235
	s_waitcnt lgkmcnt(0)
	v_max_f32_e32 v236, v236, v236
	v_max_f32_e32 v229, v229, v236
	v_cndmask_b32_e32 v235, v235, v237, vcc
	v_sqrt_f32_e32 v237, v235
	v_mul_f32_e32 v229, 0x3e088889, v229
	v_add_u32_e32 v236, -1, v237
	v_fma_f32 v238, -v236, v237, v235
	v_cmp_ge_f32_e64 s[88:89], 0, v238
	v_add_u32_e32 v238, 1, v237
	s_nop 0
	v_cndmask_b32_e64 v236, v237, v236, s[88:89]
	v_fma_f32 v237, -v238, v237, v235
	v_cmp_lt_f32_e64 s[88:89], 0, v237
	s_nop 1
	v_cndmask_b32_e64 v236, v236, v238, s[88:89]
	v_mul_f32_e32 v237, 0x37800000, v236
	v_cndmask_b32_e32 v236, v236, v237, vcc
	v_cmp_class_f32_e32 vcc, v235, v233
	s_nop 1
	v_cndmask_b32_e32 v235, v236, v235, vcc
	v_mul_f32_e32 v235, 0x3eab9f56, v235
	v_min_f32_e32 v229, v235, v229
	v_max_f32_e32 v235, 0xda24260, v229
	v_div_scale_f32 v229, s[88:89], v235, v235, 1.0
	v_rcp_f32_e32 v236, v229
	s_nop 0
	v_fma_f32 v237, -v229, v236, 1.0
	v_fmac_f32_e32 v236, v237, v236
	v_div_scale_f32 v237, vcc, 1.0, v235, 1.0
	v_mul_f32_e32 v238, v237, v236
	v_fma_f32 v239, -v229, v238, v237
	v_fmac_f32_e32 v238, v239, v236
	v_fma_f32 v229, -v229, v238, v237
	v_div_fmas_f32 v229, v229, v236, v238
	v_div_fixup_f32 v229, v229, v235, 1.0
	v_mul_f32_e32 v179, v179, v229
	v_mul_f32_e32 v178, v178, v229
	v_floor_f32_e32 v179, v179
	v_mul_f32_e32 v180, v180, v229
	v_floor_f32_e32 v178, v178
	v_add_f32_e32 v179, 0x41000000, v179
	v_floor_f32_e32 v180, v180
	v_add_f32_e32 v178, 0x41000000, v178
	v_med3_f32 v179, v179, 0, v234
	v_add_f32_e32 v180, 0x41000000, v180
	v_med3_f32 v178, v178, 0, v234
	v_cvt_i32_f32_e32 v179, v179
	v_med3_f32 v180, v180, 0, v234
	v_cvt_i32_f32_e32 v178, v178
	v_cvt_i32_f32_sdwa v180, v180 dst_sel:WORD_1 dst_unused:UNUSED_PAD src0_sel:DWORD
	v_lshlrev_b32_e32 v179, 8, v179
	v_mul_f32_e32 v171, v171, v229
	v_mul_f32_e32 v170, v170, v229
	v_or3_b32 v178, v179, v178, v180
	v_mul_f32_e32 v179, v181, v229
	v_mul_f32_e32 v181, v183, v229
	v_floor_f32_e32 v179, v179
	v_mul_f32_e32 v180, v182, v229
	v_floor_f32_e32 v181, v181
	v_mul_f32_e32 v182, v184, v229
	v_add_f32_e32 v179, 0x41000000, v179
	v_floor_f32_e32 v180, v180
	v_add_f32_e32 v181, 0x41000000, v181
	v_floor_f32_e32 v182, v182
	v_mul_f32_e32 v183, v185, v229
	v_floor_f32_e32 v171, v171
	v_mul_f32_e32 v172, v172, v229
	v_med3_f32 v179, v179, 0, v234
	v_add_f32_e32 v180, 0x41000000, v180
	v_med3_f32 v181, v181, 0, v234
	v_add_f32_e32 v182, 0x41000000, v182
	v_floor_f32_e32 v183, v183
	v_floor_f32_e32 v170, v170
	v_add_f32_e32 v171, 0x41000000, v171
	v_floor_f32_e32 v172, v172
	v_mul_f32_e32 v175, v175, v229
	v_cvt_i32_f32_sdwa v179, v179 dst_sel:BYTE_3 dst_unused:UNUSED_PAD src0_sel:DWORD
	v_med3_f32 v180, v180, 0, v234
	v_cvt_i32_f32_e32 v181, v181
	v_med3_f32 v182, v182, 0, v234
	v_add_f32_e32 v183, 0x41000000, v183
	v_add_f32_e32 v170, 0x41000000, v170
	v_med3_f32 v171, v171, 0, v234
	v_add_f32_e32 v172, 0x41000000, v172
	v_mul_f32_e32 v174, v174, v229
	v_floor_f32_e32 v175, v175
	v_mul_f32_e32 v176, v176, v229
	v_cvt_i32_f32_e32 v180, v180
	v_cvt_i32_f32_sdwa v182, v182 dst_sel:WORD_1 dst_unused:UNUSED_PAD src0_sel:DWORD
	v_med3_f32 v183, v183, 0, v234
	v_med3_f32 v170, v170, 0, v234
	v_cvt_i32_f32_e32 v171, v171
	v_med3_f32 v172, v172, 0, v234
	v_floor_f32_e32 v174, v174
	v_add_f32_e32 v175, 0x41000000, v175
	v_floor_f32_e32 v176, v176
	v_cvt_i32_f32_sdwa v183, v183 dst_sel:BYTE_3 dst_unused:UNUSED_PAD src0_sel:DWORD
	v_cvt_i32_f32_e32 v170, v170
	v_cvt_i32_f32_sdwa v172, v172 dst_sel:WORD_1 dst_unused:UNUSED_PAD src0_sel:DWORD
	v_add_f32_e32 v174, 0x41000000, v174
	v_med3_f32 v175, v175, 0, v234
	v_add_f32_e32 v176, 0x41000000, v176
	v_med3_f32 v174, v174, 0, v234
	v_cvt_i32_f32_e32 v175, v175
	v_med3_f32 v176, v176, 0, v234
	v_bitop3_b32 v178, v178, s77, v179 bitop3:0x36
	v_lshlrev_b32_e32 v179, 8, v181
	v_cvt_i32_f32_e32 v174, v174
	v_cvt_i32_f32_sdwa v176, v176 dst_sel:WORD_1 dst_unused:UNUSED_PAD src0_sel:DWORD
	v_or3_b32 v179, v179, v180, v182
	v_lshlrev_b32_e32 v171, 8, v171
	v_or_b32_e32 v180, v179, v183
	v_bitop3_b32 v179, v179, s77, v183 bitop3:0x36
	v_or3_b32 v170, v171, v170, v172
	v_mul_f32_e32 v171, v173, v229
	v_mul_f32_e32 v173, v223, v229
	v_cndmask_b32_e64 v179, v179, v180, s[86:87]
	v_floor_f32_e32 v171, v171
	v_mul_f32_e32 v172, v222, v229
	v_floor_f32_e32 v173, v173
	v_mul_f32_e32 v180, v224, v229
	v_lshlrev_b32_e32 v175, 8, v175
	v_add_f32_e32 v171, 0x41000000, v171
	v_floor_f32_e32 v172, v172
	v_add_f32_e32 v173, 0x41000000, v173
	v_floor_f32_e32 v180, v180
	v_or3_b32 v174, v175, v174, v176
	v_mul_f32_e32 v175, v177, v229
	v_mul_f32_e32 v167, v167, v229
	v_med3_f32 v171, v171, 0, v234
	v_add_f32_e32 v172, 0x41000000, v172
	v_med3_f32 v173, v173, 0, v234
	v_add_f32_e32 v180, 0x41000000, v180
	v_floor_f32_e32 v175, v175
	v_mul_f32_e32 v166, v166, v229
	v_floor_f32_e32 v167, v167
	v_mul_f32_e32 v168, v168, v229
	v_cvt_i32_f32_sdwa v171, v171 dst_sel:BYTE_3 dst_unused:UNUSED_PAD src0_sel:DWORD
	v_med3_f32 v172, v172, 0, v234
	v_cvt_i32_f32_e32 v173, v173
	v_med3_f32 v180, v180, 0, v234
	v_add_f32_e32 v175, 0x41000000, v175
	v_floor_f32_e32 v166, v166
	v_add_f32_e32 v167, 0x41000000, v167
	v_floor_f32_e32 v168, v168
	v_cvt_i32_f32_e32 v172, v172
	v_cvt_i32_f32_sdwa v180, v180 dst_sel:WORD_1 dst_unused:UNUSED_PAD src0_sel:DWORD
	v_med3_f32 v175, v175, 0, v234
	v_add_f32_e32 v166, 0x41000000, v166
	v_med3_f32 v167, v167, 0, v234
	v_add_f32_e32 v168, 0x41000000, v168
	v_cvt_i32_f32_sdwa v175, v175 dst_sel:BYTE_3 dst_unused:UNUSED_PAD src0_sel:DWORD
	v_med3_f32 v166, v166, 0, v234
	v_cvt_i32_f32_e32 v167, v167
	v_med3_f32 v168, v168, 0, v234
	v_cvt_i32_f32_e32 v166, v166
	v_cvt_i32_f32_sdwa v168, v168 dst_sel:WORD_1 dst_unused:UNUSED_PAD src0_sel:DWORD
	v_mul_f32_e32 v181, v225, v229
	v_bitop3_b32 v170, v170, s77, v171 bitop3:0x36
	v_lshlrev_b32_e32 v171, 8, v173
	v_floor_f32_e32 v181, v181
	v_or3_b32 v171, v171, v172, v180
	v_mul_f32_e32 v180, v211, v229
	v_mul_f32_e32 v169, v169, v229
	v_add_f32_e32 v181, 0x41000000, v181
	v_mul_f32_e32 v173, v210, v229
	v_floor_f32_e32 v180, v180
	v_mul_f32_e32 v182, v212, v229
	v_floor_f32_e32 v169, v169
	v_bitop3_b32 v174, v174, s77, v175 bitop3:0x36
	v_lshlrev_b32_e32 v167, 8, v167
	v_mul_f32_e32 v175, v219, v229
	v_med3_f32 v181, v181, 0, v234
	v_floor_f32_e32 v173, v173
	v_add_f32_e32 v180, 0x41000000, v180
	v_floor_f32_e32 v182, v182
	v_add_f32_e32 v169, 0x41000000, v169
	v_or3_b32 v166, v167, v166, v168
	v_mul_f32_e32 v168, v218, v229
	v_floor_f32_e32 v175, v175
	v_mul_f32_e32 v176, v220, v229
	v_cvt_i32_f32_sdwa v181, v181 dst_sel:BYTE_3 dst_unused:UNUSED_PAD src0_sel:DWORD
	v_add_f32_e32 v173, 0x41000000, v173
	v_med3_f32 v180, v180, 0, v234
	v_add_f32_e32 v182, 0x41000000, v182
	v_med3_f32 v169, v169, 0, v234
	v_floor_f32_e32 v168, v168
	v_add_f32_e32 v175, 0x41000000, v175
	v_floor_f32_e32 v176, v176
	v_med3_f32 v173, v173, 0, v234
	v_cvt_i32_f32_e32 v180, v180
	v_med3_f32 v182, v182, 0, v234
	v_cvt_i32_f32_sdwa v169, v169 dst_sel:BYTE_3 dst_unused:UNUSED_PAD src0_sel:DWORD
	v_add_f32_e32 v168, 0x41000000, v168
	v_med3_f32 v175, v175, 0, v234
	v_add_f32_e32 v176, 0x41000000, v176
	v_cvt_i32_f32_e32 v173, v173
	v_cvt_i32_f32_sdwa v182, v182 dst_sel:WORD_1 dst_unused:UNUSED_PAD src0_sel:DWORD
	v_med3_f32 v168, v168, 0, v234
	v_cvt_i32_f32_e32 v175, v175
	v_med3_f32 v176, v176, 0, v234
	v_cvt_i32_f32_e32 v168, v168
	v_cvt_i32_f32_sdwa v176, v176 dst_sel:WORD_1 dst_unused:UNUSED_PAD src0_sel:DWORD
	v_or_b32_e32 v172, v171, v181
	v_bitop3_b32 v171, v171, s77, v181 bitop3:0x36
	v_cndmask_b32_e64 v171, v171, v172, s[86:87]
	v_lshlrev_b32_e32 v172, 8, v180
	v_or_b32_e32 v167, v166, v169
	v_bitop3_b32 v166, v166, s77, v169 bitop3:0x36
	v_or3_b32 v172, v172, v173, v182
	v_mul_f32_e32 v173, v213, v229
	v_mul_f32_e32 v181, v199, v229
	v_cndmask_b32_e64 v166, v166, v167, s[86:87]
	v_lshlrev_b32_e32 v167, 8, v175
	v_floor_f32_e32 v173, v173
	v_mul_f32_e32 v180, v198, v229
	v_floor_f32_e32 v181, v181
	v_mul_f32_e32 v182, v200, v229
	v_or3_b32 v167, v167, v168, v176
	v_mul_f32_e32 v168, v221, v229
	v_mul_f32_e32 v175, v215, v229
	v_add_f32_e32 v173, 0x41000000, v173
	v_floor_f32_e32 v180, v180
	v_add_f32_e32 v181, 0x41000000, v181
	v_floor_f32_e32 v182, v182
	v_mul_f32_e32 v183, v201, v229
	v_floor_f32_e32 v168, v168
	v_mul_f32_e32 v169, v214, v229
	v_floor_f32_e32 v175, v175
	v_mul_f32_e32 v176, v216, v229
	v_med3_f32 v173, v173, 0, v234
	v_add_f32_e32 v180, 0x41000000, v180
	v_med3_f32 v181, v181, 0, v234
	v_add_f32_e32 v182, 0x41000000, v182
	v_floor_f32_e32 v183, v183
	v_add_f32_e32 v168, 0x41000000, v168
	v_floor_f32_e32 v169, v169
	v_add_f32_e32 v175, 0x41000000, v175
	v_floor_f32_e32 v176, v176
	v_cvt_i32_f32_sdwa v173, v173 dst_sel:BYTE_3 dst_unused:UNUSED_PAD src0_sel:DWORD
	v_med3_f32 v180, v180, 0, v234
	v_cvt_i32_f32_e32 v181, v181
	v_med3_f32 v182, v182, 0, v234
	v_add_f32_e32 v183, 0x41000000, v183
	v_med3_f32 v168, v168, 0, v234
	v_add_f32_e32 v169, 0x41000000, v169
	v_med3_f32 v175, v175, 0, v234
	v_add_f32_e32 v176, 0x41000000, v176
	v_cvt_i32_f32_e32 v180, v180
	v_cvt_i32_f32_sdwa v182, v182 dst_sel:WORD_1 dst_unused:UNUSED_PAD src0_sel:DWORD
	v_med3_f32 v183, v183, 0, v234
	v_cvt_i32_f32_sdwa v168, v168 dst_sel:BYTE_3 dst_unused:UNUSED_PAD src0_sel:DWORD
	v_med3_f32 v169, v169, 0, v234
	v_cvt_i32_f32_e32 v175, v175
	v_med3_f32 v176, v176, 0, v234
	v_cvt_i32_f32_sdwa v183, v183 dst_sel:BYTE_3 dst_unused:UNUSED_PAD src0_sel:DWORD
	v_cvt_i32_f32_e32 v169, v169
	v_cvt_i32_f32_sdwa v176, v176 dst_sel:WORD_1 dst_unused:UNUSED_PAD src0_sel:DWORD
	v_bitop3_b32 v172, v172, s77, v173 bitop3:0x36
	v_lshlrev_b32_e32 v173, 8, v181
	v_or3_b32 v173, v173, v180, v182
	v_mul_f32_e32 v177, v217, v229
	v_bitop3_b32 v167, v167, s77, v168 bitop3:0x36
	v_lshlrev_b32_e32 v168, 8, v175
	v_or_b32_e32 v180, v173, v183
	v_bitop3_b32 v173, v173, s77, v183 bitop3:0x36
	v_floor_f32_e32 v177, v177
	v_or3_b32 v168, v168, v169, v176
	v_mul_f32_e32 v176, v203, v229
	v_cndmask_b32_e64 v173, v173, v180, s[86:87]
	v_add_f32_e32 v177, 0x41000000, v177
	v_mul_f32_e32 v175, v202, v229
	v_floor_f32_e32 v176, v176
	v_mul_f32_e32 v180, v204, v229
	v_med3_f32 v177, v177, 0, v234
	v_floor_f32_e32 v175, v175
	v_add_f32_e32 v176, 0x41000000, v176
	v_floor_f32_e32 v180, v180
	v_cvt_i32_f32_sdwa v177, v177 dst_sel:BYTE_3 dst_unused:UNUSED_PAD src0_sel:DWORD
	v_add_f32_e32 v175, 0x41000000, v175
	v_med3_f32 v176, v176, 0, v234
	v_add_f32_e32 v180, 0x41000000, v180
	v_med3_f32 v175, v175, 0, v234
	v_cvt_i32_f32_e32 v176, v176
	v_med3_f32 v180, v180, 0, v234
	v_cvt_i32_f32_e32 v175, v175
	v_cvt_i32_f32_sdwa v180, v180 dst_sel:WORD_1 dst_unused:UNUSED_PAD src0_sel:DWORD
	v_mul_f32_e32 v191, v191, v229
	v_mul_f32_e32 v190, v190, v229
	v_floor_f32_e32 v191, v191
	v_mul_f32_e32 v192, v192, v229
	v_or_b32_e32 v169, v168, v177
	v_bitop3_b32 v168, v168, s77, v177 bitop3:0x36
	v_floor_f32_e32 v190, v190
	v_add_f32_e32 v191, 0x41000000, v191
	v_floor_f32_e32 v192, v192
	v_cndmask_b32_e64 v168, v168, v169, s[86:87]
	v_lshlrev_b32_e32 v169, 8, v176
	v_add_f32_e32 v190, 0x41000000, v190
	v_med3_f32 v191, v191, 0, v234
	v_add_f32_e32 v192, 0x41000000, v192
	v_or3_b32 v169, v169, v175, v180
	v_mul_f32_e32 v175, v205, v229
	v_mul_f32_e32 v177, v195, v229
	v_med3_f32 v190, v190, 0, v234
	v_cvt_i32_f32_e32 v191, v191
	v_med3_f32 v192, v192, 0, v234
	v_floor_f32_e32 v175, v175
	v_mul_f32_e32 v176, v194, v229
	v_floor_f32_e32 v177, v177
	v_mul_f32_e32 v180, v196, v229
	v_mul_f32_e32 v163, v163, v229
	v_cvt_i32_f32_e32 v190, v190
	v_cvt_i32_f32_sdwa v192, v192 dst_sel:WORD_1 dst_unused:UNUSED_PAD src0_sel:DWORD
	v_add_f32_e32 v175, 0x41000000, v175
	v_floor_f32_e32 v176, v176
	v_add_f32_e32 v177, 0x41000000, v177
	v_floor_f32_e32 v180, v180
	v_mul_f32_e32 v181, v197, v229
	v_mul_f32_e32 v162, v162, v229
	v_floor_f32_e32 v163, v163
	v_mul_f32_e32 v164, v164, v229
	v_mul_f32_e32 v207, v207, v229
	v_med3_f32 v175, v175, 0, v234
	v_add_f32_e32 v176, 0x41000000, v176
	v_med3_f32 v177, v177, 0, v234
	v_add_f32_e32 v180, 0x41000000, v180
	v_floor_f32_e32 v181, v181
	v_floor_f32_e32 v162, v162
	v_add_f32_e32 v163, 0x41000000, v163
	v_floor_f32_e32 v164, v164
	v_mul_f32_e32 v165, v165, v229
	v_mul_f32_e32 v206, v206, v229
	v_floor_f32_e32 v207, v207
	v_mul_f32_e32 v208, v208, v229
	v_cvt_i32_f32_sdwa v175, v175 dst_sel:BYTE_3 dst_unused:UNUSED_PAD src0_sel:DWORD
	v_med3_f32 v176, v176, 0, v234
	v_cvt_i32_f32_e32 v177, v177
	v_med3_f32 v180, v180, 0, v234
	v_add_f32_e32 v181, 0x41000000, v181
	v_add_f32_e32 v162, 0x41000000, v162
	v_med3_f32 v163, v163, 0, v234
	v_add_f32_e32 v164, 0x41000000, v164
	v_floor_f32_e32 v165, v165
	v_floor_f32_e32 v206, v206
	v_add_f32_e32 v207, 0x41000000, v207
	v_floor_f32_e32 v208, v208
	v_mul_f32_e32 v209, v209, v229
	v_lshlrev_b32_e32 v191, 8, v191
	v_mul_f32_e32 v187, v187, v229
	v_cvt_i32_f32_e32 v176, v176
	v_cvt_i32_f32_sdwa v180, v180 dst_sel:WORD_1 dst_unused:UNUSED_PAD src0_sel:DWORD
	v_med3_f32 v181, v181, 0, v234
	v_med3_f32 v162, v162, 0, v234
	v_cvt_i32_f32_e32 v163, v163
	v_med3_f32 v164, v164, 0, v234
	v_add_f32_e32 v165, 0x41000000, v165
	v_add_f32_e32 v206, 0x41000000, v206
	v_med3_f32 v207, v207, 0, v234
	v_add_f32_e32 v208, 0x41000000, v208
	v_floor_f32_e32 v209, v209
	v_or3_b32 v190, v191, v190, v192
	v_mul_f32_e32 v191, v193, v229
	v_mul_f32_e32 v186, v186, v229
	v_floor_f32_e32 v187, v187
	v_mul_f32_e32 v188, v188, v229
	v_cvt_i32_f32_sdwa v181, v181 dst_sel:BYTE_3 dst_unused:UNUSED_PAD src0_sel:DWORD
	v_cvt_i32_f32_e32 v162, v162
	v_cvt_i32_f32_sdwa v164, v164 dst_sel:WORD_1 dst_unused:UNUSED_PAD src0_sel:DWORD
	v_med3_f32 v165, v165, 0, v234
	v_med3_f32 v206, v206, 0, v234
	v_cvt_i32_f32_e32 v207, v207
	v_med3_f32 v208, v208, 0, v234
	v_add_f32_e32 v209, 0x41000000, v209
	v_floor_f32_e32 v191, v191
	v_floor_f32_e32 v186, v186
	v_add_f32_e32 v187, 0x41000000, v187
	v_floor_f32_e32 v188, v188
	v_mul_f32_e32 v189, v189, v229
	v_cvt_i32_f32_sdwa v165, v165 dst_sel:BYTE_3 dst_unused:UNUSED_PAD src0_sel:DWORD
	v_cvt_i32_f32_e32 v206, v206
	v_cvt_i32_f32_sdwa v208, v208 dst_sel:WORD_1 dst_unused:UNUSED_PAD src0_sel:DWORD
	v_med3_f32 v209, v209, 0, v234
	v_add_f32_e32 v191, 0x41000000, v191
	v_add_f32_e32 v186, 0x41000000, v186
	v_med3_f32 v187, v187, 0, v234
	v_add_f32_e32 v188, 0x41000000, v188
	v_floor_f32_e32 v189, v189
	v_bitop3_b32 v169, v169, s77, v175 bitop3:0x36
	v_lshlrev_b32_e32 v175, 8, v177
	v_cvt_i32_f32_sdwa v209, v209 dst_sel:BYTE_3 dst_unused:UNUSED_PAD src0_sel:DWORD
	v_med3_f32 v191, v191, 0, v234
	v_med3_f32 v186, v186, 0, v234
	v_cvt_i32_f32_e32 v187, v187
	v_med3_f32 v188, v188, 0, v234
	v_add_f32_e32 v189, 0x41000000, v189
	v_or3_b32 v175, v175, v176, v180
	v_lshlrev_b32_e32 v163, 8, v163
	v_cvt_i32_f32_sdwa v191, v191 dst_sel:BYTE_3 dst_unused:UNUSED_PAD src0_sel:DWORD
	v_cvt_i32_f32_e32 v186, v186
	v_cvt_i32_f32_sdwa v188, v188 dst_sel:WORD_1 dst_unused:UNUSED_PAD src0_sel:DWORD
	v_med3_f32 v189, v189, 0, v234
	v_or_b32_e32 v176, v175, v181
	v_bitop3_b32 v175, v175, s77, v181 bitop3:0x36
	v_or3_b32 v162, v163, v162, v164
	v_lshlrev_b32_e32 v207, 8, v207
	v_cvt_i32_f32_sdwa v189, v189 dst_sel:BYTE_3 dst_unused:UNUSED_PAD src0_sel:DWORD
	v_cndmask_b32_e64 v175, v175, v176, s[86:87]
	v_bitop3_b32 v176, v162, s77, v165 bitop3:0x36
	v_mov_b32_e32 v162, s61
	v_mov_b32_e32 v163, s69
	v_or3_b32 v206, v207, v206, v208
	v_cndmask_b32_e64 v163, v162, v163, s[86:87]
	v_mov_b32_e32 v162, s60
	v_mov_b32_e32 v164, s68
	v_or_b32_e32 v207, v206, v209
	v_bitop3_b32 v206, v206, s77, v209 bitop3:0x36
	v_lshlrev_b32_e32 v187, 8, v187
	v_cndmask_b32_e64 v162, v162, v164, s[86:87]
	v_lshlrev_b64 v[164:165], 8, v[230:231]
	v_cndmask_b32_e64 v206, v206, v207, s[86:87]
	v_bitop3_b32 v190, v190, s77, v191 bitop3:0x36
	v_or3_b32 v186, v187, v186, v188
	v_lshl_add_u64 v[162:163], v[162:163], 0, v[164:165]
	v_mov_b32_e32 v229, v227
	v_or_b32_e32 v187, v186, v189
	v_bitop3_b32 v186, v186, s77, v189 bitop3:0x36
	v_lshl_add_u64 v[162:163], v[162:163], 0, v[228:229]
	v_lshl_or_b32 v164, v190, 4, v206
	v_cndmask_b32_e64 v186, v186, v187, s[86:87]
	global_store_dword v[162:163], v164, off
	v_add_co_u32_e32 v164, vcc, s78, v162
	v_lshl_or_b32 v177, v178, 4, v186
	s_nop 0
	v_addc_co_u32_e32 v165, vcc, 0, v163, vcc
	global_store_dword v[164:165], v177, off
	v_add_co_u32_e32 v164, vcc, s79, v162
	v_lshl_or_b32 v170, v170, 4, v179
	s_nop 0
	v_addc_co_u32_e32 v165, vcc, 0, v163, vcc
	global_store_dword v[164:165], v170, off
	v_add_co_u32_e32 v164, vcc, s80, v162
	v_lshl_or_b32 v170, v172, 4, v171
	s_nop 0
	v_addc_co_u32_e32 v165, vcc, 0, v163, vcc
	global_store_dword v[164:165], v170, off
	v_add_co_u32_e32 v164, vcc, s81, v162
	v_lshl_or_b32 v170, v174, 4, v173
	s_nop 0
	v_addc_co_u32_e32 v165, vcc, 0, v163, vcc
	global_store_dword v[164:165], v170, off
	v_add_co_u32_e32 v164, vcc, 0x1400000, v162
	v_lshl_or_b32 v166, v167, 4, v166
	s_nop 0
	v_addc_co_u32_e32 v165, vcc, 0, v163, vcc
	global_store_dword v[164:165], v166, off
	v_add_co_u32_e32 v164, vcc, 0x1800000, v162
	v_lshl_or_b32 v166, v169, 4, v168
	s_nop 0
	v_addc_co_u32_e32 v165, vcc, 0, v163, vcc
	v_add_co_u32_e32 v162, vcc, 0x1c00000, v162
	global_store_dword v[164:165], v166, off
	v_lshl_or_b32 v164, v176, 4, v175
	v_addc_co_u32_e32 v163, vcc, 0, v163, vcc
	global_store_dword v[162:163], v164, off
	s_and_saveexec_b64 s[88:89], s[82:83]
	s_cbranch_execz .Luvh_skip_scale
	v_mov_b32_e32 v162, s67
	v_mov_b32_e32 v163, s71
	v_cndmask_b32_e64 v163, v162, v163, s[86:87]
	v_mov_b32_e32 v162, s66
	v_mov_b32_e32 v164, s70
	v_cndmask_b32_e64 v162, v162, v164, s[86:87]
	v_lshl_add_u64 v[162:163], v[230:231], 2, v[162:163]
	global_store_dword v[162:163], v235, off
.Luvh_skip_scale:
	s_or_b64 exec, exec, s[88:89]
	s_cmpk_ge_u32 s47, 0xe0
	s_cbranch_scc1 .Luvh_noload
	s_add_i32 s60, s47, 32
	s_lshr_b32 s60, s60, 5
	s_lshl_b32 s61, s2, 3
	s_add_i32 s60, s60, s61
	s_addk_i32 s60, 0x800
	v_mov_b32_e32 v162, s60
	s_mov_b64 s[62:63], s[94:95]
	s_mov_b64 s[64:65], s[94:95]
	s_movk_i32 s72, 0x1000
	s_movk_i32 s73, 0x3fff
	s_movk_i32 s74, 0x2000
	s_movk_i32 s75, 0x3000
	v_lshl_add_u32 v162, v162, 3, v232
	v_add_u32_e32 v163, 0xffffc000, v162
	v_cmp_lt_i32_e64 s[86:87], s73, v162
	v_mov_b32_e32 v164, s64
	s_nop 0
	v_cndmask_b32_e64 v230, v162, v163, s[86:87]
	v_mov_b32_e32 v162, s63
	v_mov_b32_e32 v163, s65
	v_cndmask_b32_e64 v163, v162, v163, s[86:87]
	v_mov_b32_e32 v162, s62
	v_ashrrev_i32_e32 v231, 31, v230
	v_cndmask_b32_e64 v162, v162, v164, s[86:87]
	v_lshlrev_b64 v[164:165], 14, v[230:231]
	v_lshl_add_u64 v[162:163], v[162:163], 0, v[164:165]
	v_lshl_add_u64 v[162:163], v[162:163], 0, v[226:227]
	v_add_co_u32_e32 v194, vcc, s74, v162
	global_load_dwordx4 v[206:209], v[162:163], off
	global_load_dwordx4 v[190:193], v[162:163], off offset:1024
	global_load_dwordx4 v[186:189], v[162:163], off offset:2048
	global_load_dwordx4 v[178:181], v[162:163], off offset:3072
	v_addc_co_u32_e32 v195, vcc, 0, v163, vcc
	global_load_dwordx4 v[182:185], v[194:195], off offset:-4096
	v_add_co_u32_e32 v164, vcc, s72, v162
	s_nop 0
	s_nop 0
	v_addc_co_u32_e32 v165, vcc, 0, v163, vcc
	global_load_dwordx4 v[170:173], v[164:165], off offset:1024
	v_add_co_u32_e32 v196, vcc, s75, v162
	s_nop 0
	s_nop 0
	v_addc_co_u32_e32 v197, vcc, 0, v163, vcc
	global_load_dwordx4 v[222:225], v[164:165], off offset:2048
	global_load_dwordx4 v[210:213], v[164:165], off offset:3072
	global_load_dwordx4 v[198:201], v[194:195], off
	global_load_dwordx4 v[174:177], v[194:195], off offset:1024
	global_load_dwordx4 v[166:169], v[194:195], off offset:2048
	s_nop 0
	global_load_dwordx4 v[162:165], v[196:197], off offset:3072
	global_load_dwordx4 v[86:89], v[194:195], off offset:3072
	global_load_dwordx4 v[90:93], v[196:197], off
	global_load_dwordx4 v[94:97], v[196:197], off offset:1024
	global_load_dwordx4 v[98:101], v[196:197], off offset:2048
.Luvh_noload:
	s_waitcnt lgkmcnt(0)
	s_barrier
	ds_read_b128 v[2:5], v78
	ds_read_b128 v[6:9], v78 offset:64
	ds_read_b128 v[10:13], v77
	ds_read_b128 v[14:17], v77 offset:64
	s_waitcnt lgkmcnt(1)
	v_mfma_f32_16x16x32_bf16 v[2:5], v[2:5], v[10:13], 0
	ds_read_b128 v[18:21], v78 offset:128
	ds_read_b128 v[22:25], v78 offset:192
	s_waitcnt lgkmcnt(2)
	v_mfma_f32_16x16x32_bf16 v[2:5], v[6:9], v[14:17], v[2:5]
	ds_read_b128 v[6:9], v77 offset:128
	ds_read_b128 v[26:29], v77 offset:192
	s_waitcnt lgkmcnt(1)
	v_mfma_f32_16x16x32_bf16 v[2:5], v[18:21], v[6:9], v[2:5]
	s_waitcnt lgkmcnt(0)
	v_mfma_f32_16x16x32_bf16 v[2:5], v[22:25], v[26:29], v[2:5]
	s_nop 7
	ds_write_b32 v79, v2
	ds_write_b32 v79, v3 offset:1056
	ds_write_b32 v79, v4 offset:2112
	ds_write_b32 v79, v5 offset:3168
	ds_read_b128 v[2:5], v78 offset:8448
	ds_read_b128 v[18:21], v78 offset:8512
	s_waitcnt lgkmcnt(1)
	v_mfma_f32_16x16x32_bf16 v[2:5], v[2:5], v[10:13], 0
	ds_read_b128 v[10:13], v78 offset:8576
	s_waitcnt lgkmcnt(1)
	v_mfma_f32_16x16x32_bf16 v[2:5], v[18:21], v[14:17], v[2:5]
	ds_read_b128 v[14:17], v78 offset:8640
	s_waitcnt lgkmcnt(1)
	v_mfma_f32_16x16x32_bf16 v[2:5], v[10:13], v[6:9], v[2:5]
	s_waitcnt lgkmcnt(0)
	v_mfma_f32_16x16x32_bf16 v[2:5], v[14:17], v[26:29], v[2:5]
	s_nop 7
	ds_write_b32 v79, v2 offset:16896
	ds_write_b32 v79, v3 offset:17952
	ds_write_b32 v79, v4 offset:19008
	ds_write_b32 v79, v5 offset:20064
	ds_read_b128 v[2:5], v78 offset:256
	ds_read_b128 v[6:9], v78 offset:320
	ds_read_b128 v[10:13], v77 offset:34816
	ds_read_b128 v[14:17], v77 offset:34880
	s_waitcnt lgkmcnt(1)
	v_mfma_f32_16x16x32_bf16 v[2:5], v[2:5], v[10:13], 0
	ds_read_b128 v[18:21], v78 offset:384
	ds_read_b128 v[22:25], v78 offset:448
	s_waitcnt lgkmcnt(2)
	v_mfma_f32_16x16x32_bf16 v[2:5], v[6:9], v[14:17], v[2:5]
	ds_read_b128 v[6:9], v77 offset:34944
	ds_read_b128 v[26:29], v77 offset:35008
	s_waitcnt lgkmcnt(1)
	v_mfma_f32_16x16x32_bf16 v[2:5], v[18:21], v[6:9], v[2:5]
	s_waitcnt lgkmcnt(0)
	v_mfma_f32_16x16x32_bf16 v[2:5], v[22:25], v[26:29], v[2:5]
	s_nop 7
	ds_write_b32 v79, v2 offset:528
	ds_write_b32 v79, v3 offset:1584
	ds_write_b32 v79, v4 offset:2640
	ds_write_b32 v79, v5 offset:3696
	ds_read_b128 v[2:5], v78 offset:8704
	ds_read_b128 v[18:21], v78 offset:8768
	s_waitcnt lgkmcnt(1)
	v_mfma_f32_16x16x32_bf16 v[2:5], v[2:5], v[10:13], 0
	ds_read_b128 v[10:13], v78 offset:8832
	s_waitcnt lgkmcnt(1)
	v_mfma_f32_16x16x32_bf16 v[2:5], v[18:21], v[14:17], v[2:5]
	ds_read_b128 v[14:17], v78 offset:8896
	s_waitcnt lgkmcnt(1)
	v_mfma_f32_16x16x32_bf16 v[2:5], v[10:13], v[6:9], v[2:5]
	s_waitcnt lgkmcnt(0)
	v_mfma_f32_16x16x32_bf16 v[2:5], v[14:17], v[26:29], v[2:5]
	s_nop 7
	ds_write_b32 v79, v2 offset:17424
	ds_write_b32 v79, v3 offset:18480
	ds_write_b32 v79, v4 offset:19536
	ds_write_b32 v79, v5 offset:20592
	s_waitcnt lgkmcnt(0)
	s_barrier
	ds_read2_b32 v[8:9], v75 offset1:16
	ds_read2_b32 v[6:7], v75 offset0:32 offset1:48
	ds_read2_b32 v[4:5], v75 offset0:64 offset1:80
	ds_read2_b32 v[2:3], v75 offset0:96 offset1:112
	s_waitcnt lgkmcnt(3)
	v_not_b32_e32 v11, v8
	s_waitcnt lgkmcnt(2)
	v_not_b32_e32 v13, v6
	s_waitcnt lgkmcnt(1)
	v_not_b32_e32 v15, v4
	s_waitcnt lgkmcnt(0)
	v_not_b32_e32 v17, v2
	v_or_b32_e32 v25, 0x80000000, v2
	v_cmp_gt_i32_e32 vcc, 0, v2
	v_not_b32_e32 v16, v3
	v_or_b32_e32 v24, 0x80000000, v3
	v_cndmask_b32_e32 v17, v25, v17, vcc
	v_cmp_gt_i32_e32 vcc, 0, v3
	v_or_b32_e32 v23, 0x80000000, v4
	v_not_b32_e32 v14, v5
	v_cndmask_b32_e32 v16, v24, v16, vcc
	v_cmp_gt_i32_e32 vcc, 0, v4
	v_or_b32_e32 v22, 0x80000000, v5
	v_or_b32_e32 v21, 0x80000000, v6
	v_cndmask_b32_e32 v15, v23, v15, vcc
	v_cmp_gt_i32_e32 vcc, 0, v5
	v_not_b32_e32 v12, v7
	v_or_b32_e32 v20, 0x80000000, v7
	v_cndmask_b32_e32 v14, v22, v14, vcc
	v_cmp_gt_i32_e32 vcc, 0, v6
	v_or_b32_e32 v19, 0x80000000, v8
	v_not_b32_e32 v10, v9
	v_cndmask_b32_e32 v21, v21, v13, vcc
	v_cmp_gt_i32_e32 vcc, 0, v7
	v_or_b32_e32 v18, 0x80000000, v9
	s_nop 0
	v_cndmask_b32_e32 v12, v20, v12, vcc
	v_cmp_gt_i32_e32 vcc, 0, v8
	s_nop 1
	v_cndmask_b32_e32 v19, v19, v11, vcc
	v_cmp_gt_i32_e32 vcc, 0, v9
	s_nop 1
	v_cndmask_b32_e32 v18, v18, v10, vcc
	v_max_u32_e32 v10, v18, v19
	v_max3_u32 v10, v12, v21, v10
	v_max3_u32 v10, v14, v15, v10
	v_max3_u32 v10, v16, v17, v10
	s_nop 1
	v_max_u32_dpp v11, v10, v10 row_ror:8 row_mask:0xf bank_mask:0xf bound_ctrl:1
	v_min_u32_dpp v10, v10, v10 row_ror:8 row_mask:0xf bank_mask:0xf bound_ctrl:1
	s_nop 0
	v_max_u32_dpp v11, v11, v11 row_ror:4 row_mask:0xf bank_mask:0xf bound_ctrl:1
	v_min_u32_dpp v10, v10, v10 row_ror:4 row_mask:0xf bank_mask:0xf bound_ctrl:1
	s_nop 0
	v_max_u32_dpp v11, v11, v11 row_ror:2 row_mask:0xf bank_mask:0xf bound_ctrl:1
	v_min_u32_dpp v10, v10, v10 row_ror:2 row_mask:0xf bank_mask:0xf bound_ctrl:1
	s_nop 0
	v_max_u32_dpp v20, v11, v11 row_ror:1 row_mask:0xf bank_mask:0xf bound_ctrl:1
	v_min_u32_dpp v10, v10, v10 row_ror:1 row_mask:0xf bank_mask:0xf bound_ctrl:1
	v_sub_u32_e64 v22, v10, 1 clamp
	v_sub_u32_e64 v13, v14, v22 clamp
	v_sub_u32_e64 v14, v15, v22 clamp
	v_sub_u32_e64 v15, v12, v22 clamp
	v_sub_u32_e32 v12, v20, v22
	v_ffbh_u32_e32 v12, v12
	v_xor_b32_e32 v12, 31, v12
	v_sub_u32_e64 v11, v17, v22 clamp
	v_readlane_b32 s6, v12, 0
	v_readlane_b32 s7, v12, 16
	v_readlane_b32 s8, v12, 32
	s_max_i32 s6, s7, s6
	v_sub_u32_e64 v17, v18, v22 clamp
	v_readlane_b32 s9, v12, 48
	v_mov_b32_e32 v12, s8
	v_mov_b32_e32 v18, s6
	v_max3_i32 v12, s9, v12, v18
	v_cmp_lt_i32_e32 vcc, -1, v12
	v_sub_u32_e64 v10, v16, v22 clamp
	v_sub_u32_e64 v16, v21, v22 clamp
	v_sub_u32_e64 v19, v19, v22 clamp
	v_readfirstlane_b32 s16, v12
	s_mov_b64 s[6:7], -1
	s_cbranch_vccnz .LBB0_1811
	s_mov_b64 s[6:7], 0
